# adaLN partial tasks split 5:1 between lower-half and upper-half workgroups (upper half runs the WcsT fold first)
# baseline (speedup 1.0000x reference)
; __device__ void phase_prep(KParams& p, int bid, int nb, char* smem) {
;     ...
;   for (int t = bid; t < 48 * KSPLIT; t += nb) adaln_partial_task(p, t, sm);
.Lmy_A:
	s_mov_b32 s90, s2
	s_mov_b32 s100, s34
	s_movk_i32 s101, 0x5ff
	s_cmpk_lg_u32 s34, 0x200
	s_cbranch_scc1 .Lmy_A2
	s_movk_i32 s100, 0x100
	s_movk_i32 s101, 1279
	s_cmp_eq_u32 s99, 0
	s_cbranch_scc1 .Lmy_A2
	s_add_u32 s90, s2, 1024
	s_movk_i32 s101, 0x5ff
